# phase 8: the epilogue's per-row gate-weight lookup is prefetched behind the prologue loads (v210/v211) and the epilogue's dead position search removed, as in phase 9
# baseline (speedup 1.0000x reference)
.LBB0_1013:
	s_or_b64 exec, exec, s[34:35]
	s_waitcnt vmcnt(0)
	v_lshlrev_b32_e32 v3, 11, v3
	v_and_b32_e32 v3, 0x7fff800, v3
	s_lshl_b64 s[34:35], s[10:11], 22
	s_add_u32 s10, s12, s34
	s_addc_u32 s52, s13, s35
	s_lshl_b32 s34, s36, 9
	s_lshl_b32 s35, s46, 6
	s_sub_i32 s34, s35, s34
	s_ashr_i32 s35, s34, 31
	s_lshl_b64 s[36:37], s[34:35], 2
	s_add_u32 s36, s10, s36
	s_addc_u32 s37, s52, s37
	v_or_b32_e32 v146, v3, v1
	s_waitcnt lgkmcnt(0)
	v_readfirstlane_b32 s51, v2
	v_lshl_add_u64 v[2:3], s[36:37], 0, v[152:153]
	v_lshl_add_u64 v[156:157], v[2:3], 0, v[148:149]
	s_mov_b64 s[36:37], -1
	s_cmp_ge_i32 s38, s50
	v_lshl_add_u64 v[132:133], v[156:157], 0, s[22:23]
	v_lshl_add_u64 v[130:131], v[156:157], 0, s[24:25]
	v_lshl_add_u64 v[134:135], v[156:157], 0, s[26:27]
	v_lshl_add_u64 v[138:139], v[156:157], 0, s[28:29]
	v_lshl_add_u64 v[142:143], v[156:157], 0, s[30:31]
	s_cbranch_scc0 .LBB0_1017
	global_load_dwordx4 v[2:5], v[156:157], off sc1 nt
	s_mov_b32 m0, s39
	global_load_dwordx4 v[6:9], v[132:133], off sc1 nt
	v_lshl_add_u64 v[50:51], s[14:15], 0, v[146:147]
	global_load_lds_dwordx4 v146, s[14:15]
	global_load_dwordx4 v[34:37], v[130:131], off sc1 nt
	global_load_dwordx4 v[38:41], v[134:135], off sc1 nt
	s_mov_b32 m0, s40
	s_nop 0
	global_load_lds_dwordx4 v146, s[16:17]
	v_cmp_gt_i32_e32 vcc, s50, v166
	s_and_saveexec_b64 s[100:101], vcc
	s_cbranch_execz .Lp8pf_n0
	v_add_u32_e32 v204, s49, v166
	v_mov_b32_e32 v206, s48
	ds_read_b32 v206, v206 offset:32
	s_waitcnt lgkmcnt(0)
	v_cmp_gt_i32_e32 vcc, v206, v204
	s_nop 1
	v_cndmask_b32_e64 v205, 8, 0, vcc
	v_lshl_add_u32 v206, v205, 2, s48
	ds_read_b32 v206, v206 offset:16
	v_or_b32_e32 v207, 4, v205
	s_waitcnt lgkmcnt(0)
	v_cmp_gt_i32_e32 vcc, v206, v204
	s_nop 1
	v_cndmask_b32_e32 v205, v207, v205, vcc
	v_lshl_add_u32 v206, v205, 2, s48
	ds_read_b32 v206, v206 offset:8
	v_or_b32_e32 v207, 2, v205
	s_waitcnt lgkmcnt(0)
	v_cmp_gt_i32_e32 vcc, v206, v204
	s_nop 1
	v_cndmask_b32_e32 v205, v207, v205, vcc
	v_lshl_add_u32 v206, v205, 2, s48
	ds_read_b32 v206, v206 offset:4
	v_or_b32_e32 v207, 1, v205
	s_waitcnt lgkmcnt(0)
	v_cmp_gt_i32_e32 vcc, v206, v204
	s_nop 1
	v_cndmask_b32_e32 v205, v207, v205, vcc
	v_lshl_add_u32 v206, v205, 2, s48
	ds_read_b32 v206, v206
	v_add_u32_e32 v207, s47, v204
	s_waitcnt lgkmcnt(0)
	v_sub_u32_e32 v207, v207, v206
	v_lshl_add_u32 v208, v205, 9, v207
	v_ashrrev_i32_e32 v209, 31, v208
	v_lshl_add_u64 v[208:209], v[208:209], 2, s[8:9]
	global_load_dword v210, v[208:209], off
.Lp8pf_n0:
	s_or_b64 exec, exec, s[100:101]
	v_cmp_gt_i32_e32 vcc, s50, v168
	s_and_saveexec_b64 s[100:101], vcc
	s_cbranch_execz .Lp8pf_n1
	v_add_u32_e32 v204, s49, v168
	v_mov_b32_e32 v206, s48
	ds_read_b32 v206, v206 offset:32
	s_waitcnt lgkmcnt(0)
	v_cmp_gt_i32_e32 vcc, v206, v204
	s_nop 1
	v_cndmask_b32_e64 v205, 8, 0, vcc
	v_lshl_add_u32 v206, v205, 2, s48
	ds_read_b32 v206, v206 offset:16
	v_or_b32_e32 v207, 4, v205
	s_waitcnt lgkmcnt(0)
	v_cmp_gt_i32_e32 vcc, v206, v204
	s_nop 1
	v_cndmask_b32_e32 v205, v207, v205, vcc
	v_lshl_add_u32 v206, v205, 2, s48
	ds_read_b32 v206, v206 offset:8
	v_or_b32_e32 v207, 2, v205
	s_waitcnt lgkmcnt(0)
	v_cmp_gt_i32_e32 vcc, v206, v204
	s_nop 1
	v_cndmask_b32_e32 v205, v207, v205, vcc
	v_lshl_add_u32 v206, v205, 2, s48
	ds_read_b32 v206, v206 offset:4
	v_or_b32_e32 v207, 1, v205
	s_waitcnt lgkmcnt(0)
	v_cmp_gt_i32_e32 vcc, v206, v204
	s_nop 1
	v_cndmask_b32_e32 v205, v207, v205, vcc
	v_lshl_add_u32 v206, v205, 2, s48
	ds_read_b32 v206, v206
	v_add_u32_e32 v207, s47, v204
	s_waitcnt lgkmcnt(0)
	v_sub_u32_e32 v207, v207, v206
	v_lshl_add_u32 v208, v205, 9, v207
	v_ashrrev_i32_e32 v209, 31, v208
	v_lshl_add_u64 v[208:209], v[208:209], 2, s[8:9]
	global_load_dword v211, v[208:209], off
.Lp8pf_n1:
	s_or_b64 exec, exec, s[100:101]
	s_waitcnt vmcnt(4)
	s_nop 0
	v_cvt_pk_bf16_f32 v2, v2, v6
	ds_write_b32 v169, v2 offset:49152
	v_cvt_pk_bf16_f32 v2, v3, v7
	ds_write_b32 v169, v2 offset:49216
	v_cvt_pk_bf16_f32 v2, v4, v8
	ds_write_b32 v169, v2 offset:49280
	v_cvt_pk_bf16_f32 v2, v5, v9
	ds_write_b32 v169, v2 offset:49344
	global_load_dwordx4 v[42:45], v[138:139], off sc1 nt
	global_load_dwordx4 v[46:49], v[142:143], off sc1 nt
	s_waitcnt vmcnt(5)
	s_mov_b32 m0, s41
	s_waitcnt lgkmcnt(0)
	s_barrier
	global_load_lds_dwordx4 v146, s[18:19]
	v_mov_b32_e32 v2, 0
	s_mov_b32 s37, -2
	s_movk_i32 s36, 0x80
	v_mov_b32_e32 v3, v2
	v_mov_b32_e32 v4, v2
	v_mov_b32_e32 v5, v2
	v_mov_b32_e32 v6, v2
	v_mov_b32_e32 v7, v2
	v_mov_b32_e32 v8, v2
	v_mov_b32_e32 v9, v2
	v_mov_b32_e32 v10, v2
	v_mov_b32_e32 v11, v2
	v_mov_b32_e32 v12, v2
	v_mov_b32_e32 v13, v2
	v_mov_b32_e32 v14, v2
	v_mov_b32_e32 v15, v2
	v_mov_b32_e32 v16, v2
	v_mov_b32_e32 v17, v2
	v_mov_b32_e32 v66, v2
	v_mov_b32_e32 v67, v2
	v_mov_b32_e32 v68, v2
	v_mov_b32_e32 v69, v2
	v_mov_b32_e32 v70, v2
	v_mov_b32_e32 v71, v2
	v_mov_b32_e32 v72, v2
	v_mov_b32_e32 v73, v2
	v_mov_b32_e32 v74, v2
	v_mov_b32_e32 v75, v2
	v_mov_b32_e32 v76, v2
	v_mov_b32_e32 v77, v2
	v_mov_b32_e32 v78, v2
	v_mov_b32_e32 v79, v2
	v_mov_b32_e32 v80, v2
	v_mov_b32_e32 v81, v2
	v_mov_b32_e32 v18, v2
	v_mov_b32_e32 v19, v2
	v_mov_b32_e32 v20, v2
	v_mov_b32_e32 v21, v2
	v_mov_b32_e32 v22, v2
	v_mov_b32_e32 v23, v2
	v_mov_b32_e32 v24, v2
	v_mov_b32_e32 v25, v2
	v_mov_b32_e32 v26, v2
	v_mov_b32_e32 v27, v2
	v_mov_b32_e32 v28, v2
	v_mov_b32_e32 v29, v2
	v_mov_b32_e32 v30, v2
	v_mov_b32_e32 v31, v2
	v_mov_b32_e32 v32, v2
	v_mov_b32_e32 v33, v2
	v_mov_b32_e32 v114, v2
	v_mov_b32_e32 v115, v2
	v_mov_b32_e32 v116, v2
	v_mov_b32_e32 v117, v2
	v_mov_b32_e32 v118, v2
	v_mov_b32_e32 v119, v2
	v_mov_b32_e32 v120, v2
	v_mov_b32_e32 v121, v2
	v_mov_b32_e32 v122, v2
	v_mov_b32_e32 v123, v2
	v_mov_b32_e32 v124, v2
	v_mov_b32_e32 v125, v2
	v_mov_b32_e32 v126, v2
	v_mov_b32_e32 v127, v2
	v_mov_b32_e32 v128, v2
	v_mov_b32_e32 v129, v2
	v_readfirstlane_b32 s98, v250
	s_bitcmp1_b32 s98, 6
	s_cbranch_scc1 .Lmoe_B_1015

.LBB0_1017:
	v_mov_b32_e32 v97, 0
	s_and_b64 vcc, exec, s[36:37]
	v_mov_b32_e32 v96, v97
	v_mov_b32_e32 v95, v97
	v_mov_b32_e32 v94, v97
	v_mov_b32_e32 v93, v97
	v_mov_b32_e32 v92, v97
	v_mov_b32_e32 v91, v97
	v_mov_b32_e32 v90, v97
	v_mov_b32_e32 v89, v97
	v_mov_b32_e32 v88, v97
	v_mov_b32_e32 v87, v97
	v_mov_b32_e32 v86, v97
	v_mov_b32_e32 v85, v97
	v_mov_b32_e32 v84, v97
	v_mov_b32_e32 v83, v97
	v_mov_b32_e32 v82, v97
	v_mov_b32_e32 v65, v97
	v_mov_b32_e32 v64, v97
	v_mov_b32_e32 v63, v97
	v_mov_b32_e32 v62, v97
	v_mov_b32_e32 v61, v97
	v_mov_b32_e32 v60, v97
	v_mov_b32_e32 v59, v97
	v_mov_b32_e32 v58, v97
	v_mov_b32_e32 v57, v97
	v_mov_b32_e32 v56, v97
	v_mov_b32_e32 v55, v97
	v_mov_b32_e32 v54, v97
	v_mov_b32_e32 v53, v97
	v_mov_b32_e32 v52, v97
	v_mov_b32_e32 v51, v97
	v_mov_b32_e32 v50, v97
	v_mov_b32_e32 v113, v97
	v_mov_b32_e32 v112, v97
	v_mov_b32_e32 v111, v97
	v_mov_b32_e32 v110, v97
	v_mov_b32_e32 v109, v97
	v_mov_b32_e32 v108, v97
	v_mov_b32_e32 v107, v97
	v_mov_b32_e32 v106, v97
	v_mov_b32_e32 v105, v97
	v_mov_b32_e32 v104, v97
	v_mov_b32_e32 v103, v97
	v_mov_b32_e32 v102, v97
	v_mov_b32_e32 v101, v97
	v_mov_b32_e32 v100, v97
	v_mov_b32_e32 v99, v97
	v_mov_b32_e32 v98, v97
	v_mov_b32_e32 v49, v97
	v_mov_b32_e32 v48, v97
	v_mov_b32_e32 v47, v97
	v_mov_b32_e32 v46, v97
	v_mov_b32_e32 v45, v97
	v_mov_b32_e32 v44, v97
	v_mov_b32_e32 v43, v97
	v_mov_b32_e32 v42, v97
	v_mov_b32_e32 v41, v97
	v_mov_b32_e32 v40, v97
	v_mov_b32_e32 v39, v97
	v_mov_b32_e32 v38, v97
	v_mov_b32_e32 v37, v97
	v_mov_b32_e32 v36, v97
	v_mov_b32_e32 v35, v97
	v_mov_b32_e32 v34, v97
	s_cbranch_vccz .LBB0_1021
	global_load_dwordx4 v[2:5], v[156:157], off sc1 nt
	s_mov_b32 m0, s39
	global_load_dwordx4 v[6:9], v[132:133], off sc1 nt
	v_or_b32_e32 v158, v136, v1
	global_load_lds_dwordx4 v146, s[14:15]
	s_mov_b32 m0, s42
	v_mov_b32_e32 v159, v147
	global_load_lds_dwordx4 v158, s[14:15]
	global_load_dwordx4 v[130:133], v[130:131], off sc1 nt
	global_load_dwordx4 v[134:137], v[134:135], off sc1 nt
	s_mov_b32 m0, s40
	s_nop 0
	global_load_lds_dwordx4 v146, s[16:17]
	s_mov_b32 m0, s43
	s_nop 0
	global_load_lds_dwordx4 v158, s[16:17]
	v_cmp_gt_i32_e32 vcc, s50, v166
	s_and_saveexec_b64 s[100:101], vcc
	s_cbranch_execz .Lp8pf_t0
	v_add_u32_e32 v204, s49, v166
	v_mov_b32_e32 v206, s48
	ds_read_b32 v206, v206 offset:32
	s_waitcnt lgkmcnt(0)
	v_cmp_gt_i32_e32 vcc, v206, v204
	s_nop 1
	v_cndmask_b32_e64 v205, 8, 0, vcc
	v_lshl_add_u32 v206, v205, 2, s48
	ds_read_b32 v206, v206 offset:16
	v_or_b32_e32 v207, 4, v205
	s_waitcnt lgkmcnt(0)
	v_cmp_gt_i32_e32 vcc, v206, v204
	s_nop 1
	v_cndmask_b32_e32 v205, v207, v205, vcc
	v_lshl_add_u32 v206, v205, 2, s48
	ds_read_b32 v206, v206 offset:8
	v_or_b32_e32 v207, 2, v205
	s_waitcnt lgkmcnt(0)
	v_cmp_gt_i32_e32 vcc, v206, v204
	s_nop 1
	v_cndmask_b32_e32 v205, v207, v205, vcc
	v_lshl_add_u32 v206, v205, 2, s48
	ds_read_b32 v206, v206 offset:4
	v_or_b32_e32 v207, 1, v205
	s_waitcnt lgkmcnt(0)
	v_cmp_gt_i32_e32 vcc, v206, v204
	s_nop 1
	v_cndmask_b32_e32 v205, v207, v205, vcc
	v_lshl_add_u32 v206, v205, 2, s48
	ds_read_b32 v206, v206
	v_add_u32_e32 v207, s47, v204
	s_waitcnt lgkmcnt(0)
	v_sub_u32_e32 v207, v207, v206
	v_lshl_add_u32 v208, v205, 9, v207
	v_ashrrev_i32_e32 v209, 31, v208
	v_lshl_add_u64 v[208:209], v[208:209], 2, s[8:9]
	global_load_dword v210, v[208:209], off

.Lp8pf_t1:
	s_or_b64 exec, exec, s[100:101]
	s_waitcnt vmcnt(6)
	s_nop 0
	v_cvt_pk_bf16_f32 v2, v2, v6
	ds_write_b32 v169, v2 offset:49152
	v_cvt_pk_bf16_f32 v2, v3, v7
	ds_write_b32 v169, v2 offset:49216
	v_cvt_pk_bf16_f32 v2, v4, v8
	ds_write_b32 v169, v2 offset:49280
	v_cvt_pk_bf16_f32 v2, v5, v9
	ds_write_b32 v169, v2 offset:49344
	global_load_dwordx4 v[138:141], v[138:139], off sc1 nt
	global_load_dwordx4 v[142:145], v[142:143], off sc1 nt
	s_waitcnt vmcnt(6)
	s_mov_b32 m0, s41
	s_waitcnt lgkmcnt(0)
	s_barrier
	global_load_lds_dwordx4 v146, s[18:19]
	s_mov_b32 m0, s44
	v_mov_b32_e32 v34, 0
	global_load_lds_dwordx4 v158, s[18:19]
	s_mov_b32 s37, -2
	s_movk_i32 s36, 0x80
	v_mov_b32_e32 v35, v34
	v_mov_b32_e32 v36, v34
	v_mov_b32_e32 v37, v34
	v_mov_b32_e32 v38, v34
	v_mov_b32_e32 v39, v34
	v_mov_b32_e32 v40, v34
	v_mov_b32_e32 v41, v34
	v_mov_b32_e32 v42, v34
	v_mov_b32_e32 v43, v34
	v_mov_b32_e32 v44, v34
	v_mov_b32_e32 v45, v34
	v_mov_b32_e32 v46, v34
	v_mov_b32_e32 v47, v34
	v_mov_b32_e32 v48, v34
	v_mov_b32_e32 v49, v34
	v_mov_b32_e32 v98, v34
	v_mov_b32_e32 v99, v34
	v_mov_b32_e32 v100, v34
	v_mov_b32_e32 v101, v34
	v_mov_b32_e32 v102, v34
	v_mov_b32_e32 v103, v34
	v_mov_b32_e32 v104, v34
	v_mov_b32_e32 v105, v34
	v_mov_b32_e32 v106, v34
	v_mov_b32_e32 v107, v34
	v_mov_b32_e32 v108, v34
	v_mov_b32_e32 v109, v34
	v_mov_b32_e32 v110, v34
	v_mov_b32_e32 v111, v34
	v_mov_b32_e32 v112, v34
	v_mov_b32_e32 v113, v34
	v_mov_b32_e32 v50, v34
	v_mov_b32_e32 v51, v34
	v_mov_b32_e32 v52, v34
	v_mov_b32_e32 v53, v34
	v_mov_b32_e32 v54, v34
	v_mov_b32_e32 v55, v34
	v_mov_b32_e32 v56, v34
	v_mov_b32_e32 v57, v34
	v_mov_b32_e32 v58, v34
	v_mov_b32_e32 v59, v34
	v_mov_b32_e32 v60, v34
	v_mov_b32_e32 v61, v34
	v_mov_b32_e32 v62, v34
	v_mov_b32_e32 v63, v34
	v_mov_b32_e32 v64, v34
	v_mov_b32_e32 v65, v34
	v_mov_b32_e32 v82, v34
	v_mov_b32_e32 v83, v34
	v_mov_b32_e32 v84, v34
	v_mov_b32_e32 v85, v34
	v_mov_b32_e32 v86, v34
	v_mov_b32_e32 v87, v34
	v_mov_b32_e32 v88, v34
	v_mov_b32_e32 v89, v34
	v_mov_b32_e32 v90, v34
	v_mov_b32_e32 v91, v34
	v_mov_b32_e32 v92, v34
	v_mov_b32_e32 v93, v34
	v_mov_b32_e32 v94, v34
	v_mov_b32_e32 v95, v34
	v_mov_b32_e32 v96, v34
	v_mov_b32_e32 v97, v34
	v_mov_b32_e32 v2, v34
	v_mov_b32_e32 v3, v34
	v_mov_b32_e32 v4, v34
	v_mov_b32_e32 v5, v34
	v_mov_b32_e32 v6, v34
	v_mov_b32_e32 v7, v34
	v_mov_b32_e32 v8, v34
	v_mov_b32_e32 v9, v34
	v_mov_b32_e32 v10, v34
	v_mov_b32_e32 v11, v34
	v_mov_b32_e32 v12, v34
	v_mov_b32_e32 v13, v34
	v_mov_b32_e32 v14, v34
	v_mov_b32_e32 v15, v34
	v_mov_b32_e32 v16, v34
	v_mov_b32_e32 v17, v34
	v_mov_b32_e32 v66, v34
	v_mov_b32_e32 v67, v34
	v_mov_b32_e32 v68, v34
	v_mov_b32_e32 v69, v34
	v_mov_b32_e32 v70, v34
	v_mov_b32_e32 v71, v34
	v_mov_b32_e32 v72, v34
	v_mov_b32_e32 v73, v34
	v_mov_b32_e32 v74, v34
	v_mov_b32_e32 v75, v34
	v_mov_b32_e32 v76, v34
	v_mov_b32_e32 v77, v34
	v_mov_b32_e32 v78, v34
	v_mov_b32_e32 v79, v34
	v_mov_b32_e32 v80, v34
	v_mov_b32_e32 v81, v34
	v_mov_b32_e32 v18, v34
	v_mov_b32_e32 v19, v34
	v_mov_b32_e32 v20, v34
	v_mov_b32_e32 v21, v34
	v_mov_b32_e32 v22, v34
	v_mov_b32_e32 v23, v34
	v_mov_b32_e32 v24, v34
	v_mov_b32_e32 v25, v34
	v_mov_b32_e32 v26, v34
	v_mov_b32_e32 v27, v34
	v_mov_b32_e32 v28, v34
	v_mov_b32_e32 v29, v34
	v_mov_b32_e32 v30, v34
	v_mov_b32_e32 v31, v34
	v_mov_b32_e32 v32, v34
	v_mov_b32_e32 v33, v34
	v_mov_b32_e32 v114, v34
	v_mov_b32_e32 v115, v34
	v_mov_b32_e32 v116, v34
	v_mov_b32_e32 v117, v34
	v_mov_b32_e32 v118, v34
	v_mov_b32_e32 v119, v34
	v_mov_b32_e32 v120, v34
	v_mov_b32_e32 v121, v34
	v_mov_b32_e32 v122, v34
	v_mov_b32_e32 v123, v34
	v_mov_b32_e32 v124, v34
	v_mov_b32_e32 v125, v34
	v_mov_b32_e32 v126, v34
	v_mov_b32_e32 v127, v34
	v_mov_b32_e32 v128, v34
	v_mov_b32_e32 v129, v34
	v_readfirstlane_b32 s98, v250
	s_bitcmp1_b32 s98, 6
	s_cbranch_scc1 .Lmoe_B_1019

.LBB0_1021:
	s_waitcnt vmcnt(0)
	s_add_i32 s51, s51, s49
	v_cmp_gt_i32_e32 vcc, s50, v166
	s_and_saveexec_b64 s[36:37], vcc
	s_cbranch_execz .LBB0_1023
	v_mov_b32_e32 v130, s48

	v_add_u32_e32 v131, s49, v166
	v_mul_f32_e32 v136, 0xbfb8aa3b, v114
	v_mul_f32_e32 v137, 0xbfb8aa3b, v115
	v_mul_f32_e32 v138, 0xbfb8aa3b, v116
	s_waitcnt lgkmcnt(0)
	v_cmp_gt_i32_e32 vcc, v130, v131
	v_mov_b32_e32 v134, v68
	v_mul_f32_e32 v68, 0xbfb8aa3b, v117
	v_cndmask_b32_e64 v130, 8, 0, vcc
	v_lshl_add_u32 v132, v130, 2, s48

	v_or_b32_e32 v133, 4, v130
	v_mul_f32_e32 v139, 0xbfb8aa3b, v118
	v_mul_f32_e32 v140, 0xbfb8aa3b, v119
	v_mul_f32_e32 v141, 0xbfb8aa3b, v120
	s_waitcnt lgkmcnt(0)
	v_cmp_gt_i32_e32 vcc, v132, v131
	v_mul_f32_e32 v142, 0xbfb8aa3b, v121
	v_mul_f32_e32 v143, 0xbfb8aa3b, v122
	v_cndmask_b32_e32 v130, v133, v130, vcc
	v_lshl_add_u32 v132, v130, 2, s48

	v_or_b32_e32 v133, 2, v130
	v_mul_f32_e32 v144, 0xbfb8aa3b, v123
	v_exp_f32_e32 v136, v136
	v_exp_f32_e32 v137, v137
	s_waitcnt lgkmcnt(0)
	v_cmp_gt_i32_e32 vcc, v132, v131
	v_exp_f32_e32 v138, v138
	v_exp_f32_e32 v68, v68
	v_cndmask_b32_e32 v130, v133, v130, vcc
	v_lshl_add_u32 v132, v130, 2, s48

	v_or_b32_e32 v133, 1, v130
	v_exp_f32_e32 v139, v139
	v_exp_f32_e32 v140, v140
	v_exp_f32_e32 v141, v141
	s_waitcnt lgkmcnt(0)
	v_cmp_gt_i32_e32 vcc, v132, v131
	v_add_u32_e32 v131, s47, v131
	v_exp_f32_e32 v142, v142
	v_cndmask_b32_e32 v130, v133, v130, vcc
	v_lshl_add_u32 v132, v130, 2, s48

	v_exp_f32_e32 v143, v143
	v_exp_f32_e32 v144, v144
	v_add_f32_e32 v136, 1.0, v136
	v_add_f32_e32 v137, 1.0, v137
	s_waitcnt lgkmcnt(0)
	v_sub_u32_e32 v131, v131, v132
	v_lshl_add_u32 v130, v130, 9, v131
	v_ashrrev_i32_e32 v131, 31, v130
	v_lshl_add_u64 v[130:131], v[130:131], 2, s[8:9]
	v_mov_b32_e32 v135, v210
	v_add_f32_e32 v138, 1.0, v138
	v_add_f32_e32 v68, 1.0, v68
	v_add_f32_e32 v139, 1.0, v139
	v_add_f32_e32 v140, 1.0, v140
	v_add_f32_e32 v141, 1.0, v141
	v_add_f32_e32 v142, 1.0, v142
	v_add_f32_e32 v143, 1.0, v143
	v_add_f32_e32 v144, 1.0, v144
	v_rcp_f32_e32 v136, v136
	v_rcp_f32_e32 v137, v137
	v_rcp_f32_e32 v138, v138
	v_rcp_f32_e32 v68, v68
	v_rcp_f32_e32 v139, v139
	v_rcp_f32_e32 v140, v140
	v_rcp_f32_e32 v141, v141
	v_rcp_f32_e32 v142, v142
	v_rcp_f32_e32 v143, v143
	v_rcp_f32_e32 v144, v144
	v_mul_f32_e32 v114, v114, v136
	v_mul_f32_e32 v115, v115, v137
	v_mul_f32_e32 v154, v116, v138
	v_mul_f32_e32 v68, v117, v68
	v_mul_f32_e32 v116, v118, v139
	v_mul_f32_e32 v117, v119, v140
	v_mul_f32_e32 v118, v120, v141
	v_mul_f32_e32 v119, v121, v142
	v_mul_f32_e32 v120, v122, v143
	v_mul_f32_e32 v121, v123, v144
	v_mul_f32_e32 v114, v66, v114
	v_mul_f32_e32 v115, v67, v115
	v_mul_f32_e32 v145, 0xbfb8aa3b, v124
	v_mul_f32_e32 v146, 0xbfb8aa3b, v125
	v_mul_f32_e32 v68, v69, v68
	v_mul_f32_e32 v69, v70, v116
	v_mul_f32_e32 v70, v71, v117
	v_mul_f32_e32 v71, v72, v118
	v_mul_f32_e32 v72, v73, v119
	v_mul_f32_e32 v73, v74, v120
	v_mul_f32_e32 v74, v75, v121
	v_mov_b32_e32 v132, v147
	v_exp_f32_e32 v145, v145
	v_exp_f32_e32 v146, v146
	v_mov_b32_e32 v133, v147
	v_add_u32_e32 v130, s51, v166
	v_add_f32_e32 v145, 1.0, v145
	v_add_f32_e32 v146, 1.0, v146
	v_rcp_f32_e32 v145, v145
	v_ashrrev_i32_e32 v131, 31, v130
	v_lshlrev_b64 v[130:131], 9, v[130:131]
	v_lshl_add_u64 v[130:131], s[20:21], 0, v[130:131]
	v_lshl_add_u64 v[130:131], v[130:131], 0, s[34:35]
	v_lshl_add_u64 v[130:131], v[130:131], 0, v[150:151]
	s_waitcnt vmcnt(0)
	v_pk_mul_f32 v[66:67], v[134:135], v[154:155]
	s_nop 0
	v_mul_f32_e32 v75, v114, v67
	v_mul_f32_e32 v114, v115, v67
	v_med3_f32 v75, v75, s45, v170
	v_med3_f32 v114, v114, s45, v170
	v_mul_f32_e32 v69, v69, v67
	v_mul_f32_e32 v70, v70, v67
	v_cvt_pk_fp8_f32 v132, v75, v114
	v_mul_f32_e32 v71, v71, v67
	v_med3_f32 v69, v69, s45, v170
	v_med3_f32 v70, v70, s45, v170
	v_mul_f32_e32 v66, v66, v67
	v_mul_f32_e32 v68, v68, v67
	v_cvt_pk_fp8_f32 v133, v69, v70
	v_med3_f32 v69, v71, s45, v170
	v_mul_f32_e32 v71, 0xbfb8aa3b, v126
	v_med3_f32 v66, v66, s45, v170
	v_med3_f32 v68, v68, s45, v170
	v_exp_f32_e32 v71, v71
	v_mul_f32_e32 v72, v72, v67
	v_cvt_pk_fp8_f32 v132, v66, v68 op_sel:[0,0,1]
	v_rcp_f32_e32 v66, v146
	v_mul_f32_e32 v73, v73, v67
	v_mul_f32_e32 v74, v74, v67
	v_med3_f32 v70, v72, s45, v170
	v_cvt_pk_fp8_f32 v133, v69, v70 op_sel:[0,0,1]
	v_med3_f32 v69, v73, s45, v170
	v_med3_f32 v70, v74, s45, v170
	v_mov_b32_e32 v134, v147
	v_cvt_pk_fp8_f32 v134, v69, v70
	v_mul_f32_e32 v69, 0xbfb8aa3b, v127
	v_add_f32_e32 v70, 1.0, v71
	v_mul_f32_e32 v68, v124, v145
	v_mul_f32_e32 v66, v125, v66
	v_exp_f32_e32 v69, v69
	v_rcp_f32_e32 v70, v70
	v_mul_f32_e32 v68, v76, v68
	v_mul_f32_e32 v66, v77, v66
	v_mul_f32_e32 v68, v68, v67
	v_mul_f32_e32 v66, v66, v67
	v_med3_f32 v68, v68, s45, v170
	v_med3_f32 v66, v66, s45, v170
	v_cvt_pk_fp8_f32 v134, v68, v66 op_sel:[0,0,1]
	v_add_f32_e32 v66, 1.0, v69
	v_mul_f32_e32 v68, v126, v70
	v_mul_f32_e32 v69, 0xbfb8aa3b, v128
	v_mul_f32_e32 v70, 0xbfb8aa3b, v129
	v_exp_f32_e32 v69, v69
	v_exp_f32_e32 v70, v70
	v_rcp_f32_e32 v66, v66
	v_mul_f32_e32 v68, v78, v68
	v_add_f32_e32 v69, 1.0, v69
	v_add_f32_e32 v70, 1.0, v70
	v_mul_f32_e32 v66, v127, v66
	v_rcp_f32_e32 v69, v69
	v_rcp_f32_e32 v70, v70
	v_mul_f32_e32 v66, v79, v66
	v_mul_f32_e32 v68, v68, v67
	v_mul_f32_e32 v66, v66, v67
	v_med3_f32 v68, v68, s45, v170
	v_med3_f32 v66, v66, s45, v170
	v_mov_b32_e32 v135, v147
	v_mul_f32_e32 v69, v128, v69
	v_mul_f32_e32 v70, v129, v70
	v_cvt_pk_fp8_f32 v135, v68, v66
	v_mul_f32_e32 v69, v80, v69
	v_mul_f32_e32 v70, v81, v70
	v_mul_f32_e32 v69, v69, v67
	v_mul_f32_e32 v66, v70, v67
	v_med3_f32 v68, v69, s45, v170
	v_med3_f32 v66, v66, s45, v170
	v_cvt_pk_fp8_f32 v135, v68, v66 op_sel:[0,0,1]
	v_mul_f32_e32 v66, 0xbfb8aa3b, v18
	v_exp_f32_e32 v66, v66
	v_mul_f32_e32 v68, 0xbfb8aa3b, v19
	v_exp_f32_e32 v68, v68
	v_permlane32_swap_b32_e32 v132, v133
	v_add_f32_e32 v66, 1.0, v66
	v_rcp_f32_e32 v66, v66
	v_add_f32_e32 v68, 1.0, v68
	v_rcp_f32_e32 v68, v68
	v_permlane32_swap_b32_e32 v134, v135
	v_mul_f32_e32 v18, v18, v66
	v_mul_f32_e32 v2, v2, v18
	v_mul_f32_e32 v18, v19, v68
	v_mul_f32_e32 v3, v3, v18
	v_mul_f32_e32 v18, 0xbfb8aa3b, v21
	v_mul_f32_e32 v19, 0xbfb8aa3b, v20
	v_exp_f32_e32 v18, v18
	v_exp_f32_e32 v19, v19
	v_mul_f32_e32 v2, v2, v67
	v_mul_f32_e32 v3, v3, v67
	v_add_f32_e32 v18, 1.0, v18
	v_add_f32_e32 v19, 1.0, v19
	v_rcp_f32_e32 v18, v18
	v_rcp_f32_e32 v19, v19
	v_med3_f32 v3, v3, s45, v170
	v_permlane32_swap_b32_e32 v132, v134
	v_mul_f32_e32 v18, v21, v18
	v_mul_f32_e32 v19, v20, v19
	v_mul_f32_e32 v5, v5, v18
	v_med3_f32 v18, v2, s45, v170
	v_mov_b32_e32 v2, v147
	v_mul_f32_e32 v4, v4, v19
	v_mul_f32_e32 v19, 0xbfb8aa3b, v22
	v_cvt_pk_fp8_f32 v2, v18, v3
	v_exp_f32_e32 v19, v19
	v_mul_f32_e32 v4, v4, v67
	v_mul_f32_e32 v5, v5, v67
	v_med3_f32 v4, v4, s45, v170
	v_med3_f32 v5, v5, s45, v170
	v_cvt_pk_fp8_f32 v2, v4, v5 op_sel:[0,0,1]
	v_mul_f32_e32 v5, 0xbfb8aa3b, v24
	v_add_f32_e32 v18, 1.0, v19
	v_exp_f32_e32 v5, v5
	v_mul_f32_e32 v3, 0xbfb8aa3b, v23
	v_rcp_f32_e32 v18, v18
	v_exp_f32_e32 v3, v3
	v_add_f32_e32 v5, 1.0, v5
	v_rcp_f32_e32 v5, v5
	v_mul_f32_e32 v4, v22, v18
	v_add_f32_e32 v3, 1.0, v3
	v_mul_f32_e32 v4, v6, v4
	v_mul_f32_e32 v6, 0xbfb8aa3b, v25
	v_rcp_f32_e32 v3, v3
	v_exp_f32_e32 v6, v6
	v_mul_f32_e32 v5, v24, v5
	v_mul_f32_e32 v5, v8, v5
	v_mul_f32_e32 v8, 0xbfb8aa3b, v26
	v_mul_f32_e32 v3, v23, v3
	v_add_f32_e32 v6, 1.0, v6
	v_exp_f32_e32 v8, v8
	v_mul_f32_e32 v3, v7, v3
	v_rcp_f32_e32 v6, v6
	v_mul_f32_e32 v4, v4, v67
	v_mul_f32_e32 v3, v3, v67
	v_med3_f32 v4, v4, s45, v170
	v_med3_f32 v7, v3, s45, v170
	v_mov_b32_e32 v3, v147
	v_cvt_pk_fp8_f32 v3, v4, v7
	v_mul_f32_e32 v4, 0xbfb8aa3b, v27
	v_add_f32_e32 v7, 1.0, v8
	v_mul_f32_e32 v6, v25, v6
	v_exp_f32_e32 v4, v4
	v_rcp_f32_e32 v7, v7
	v_mul_f32_e32 v6, v9, v6
	v_mul_f32_e32 v5, v5, v67
	v_mul_f32_e32 v6, v6, v67
	v_med3_f32 v5, v5, s45, v170
	v_med3_f32 v6, v6, s45, v170
	v_cvt_pk_fp8_f32 v3, v5, v6 op_sel:[0,0,1]
	v_add_f32_e32 v4, 1.0, v4
	v_mul_f32_e32 v5, v26, v7
	v_mul_f32_e32 v6, 0xbfb8aa3b, v28
	v_mul_f32_e32 v7, 0xbfb8aa3b, v29
	v_rcp_f32_e32 v4, v4
	v_exp_f32_e32 v6, v6
	v_exp_f32_e32 v7, v7
	v_mul_f32_e32 v9, 0xbfb8aa3b, v30
	v_mul_f32_e32 v4, v27, v4
	v_add_f32_e32 v6, 1.0, v6
	v_add_f32_e32 v7, 1.0, v7
	v_exp_f32_e32 v9, v9
	v_mul_f32_e32 v5, v10, v5
	v_mul_f32_e32 v4, v11, v4
	v_rcp_f32_e32 v6, v6
	v_rcp_f32_e32 v7, v7
	v_mul_f32_e32 v5, v5, v67
	v_mul_f32_e32 v4, v4, v67
	v_med3_f32 v5, v5, s45, v170
	v_med3_f32 v8, v4, s45, v170
	v_mov_b32_e32 v4, v147
	v_cvt_pk_fp8_f32 v4, v5, v8
	v_add_f32_e32 v8, 1.0, v9
	v_mul_f32_e32 v6, v28, v6
	v_mul_f32_e32 v7, v29, v7
	v_mul_f32_e32 v5, 0xbfb8aa3b, v31
	v_rcp_f32_e32 v8, v8
	v_mul_f32_e32 v6, v12, v6
	v_mul_f32_e32 v7, v13, v7
	v_exp_f32_e32 v5, v5
	v_mul_f32_e32 v6, v6, v67
	v_mul_f32_e32 v7, v7, v67
	v_med3_f32 v6, v6, s45, v170
	v_med3_f32 v7, v7, s45, v170
	v_cvt_pk_fp8_f32 v4, v6, v7 op_sel:[0,0,1]
	v_mul_f32_e32 v6, v30, v8
	v_mul_f32_e32 v7, 0xbfb8aa3b, v32
	v_mul_f32_e32 v8, 0xbfb8aa3b, v33
	v_add_f32_e32 v5, 1.0, v5
	v_exp_f32_e32 v7, v7
	v_exp_f32_e32 v8, v8
	v_rcp_f32_e32 v5, v5
	v_mul_f32_e32 v6, v14, v6
	v_add_f32_e32 v7, 1.0, v7
	v_add_f32_e32 v8, 1.0, v8
	v_mul_f32_e32 v5, v31, v5
	v_rcp_f32_e32 v7, v7
	v_rcp_f32_e32 v8, v8
	v_mul_f32_e32 v5, v15, v5
	v_mul_f32_e32 v6, v6, v67
	v_mul_f32_e32 v5, v5, v67
	v_med3_f32 v6, v6, s45, v170
	v_med3_f32 v9, v5, s45, v170
	v_mov_b32_e32 v5, v147
	v_mul_f32_e32 v7, v32, v7
	v_mul_f32_e32 v8, v33, v8
	v_cvt_pk_fp8_f32 v5, v6, v9
	v_mul_f32_e32 v7, v16, v7
	v_mul_f32_e32 v8, v17, v8
	v_mul_f32_e32 v7, v7, v67
	v_mul_f32_e32 v6, v8, v67
	v_med3_f32 v7, v7, s45, v170
	v_med3_f32 v6, v6, s45, v170
	v_cvt_pk_fp8_f32 v5, v7, v6 op_sel:[0,0,1]
	v_permlane32_swap_b32_e32 v2, v3
	v_permlane32_swap_b32_e32 v133, v135
	v_permlane32_swap_b32_e32 v4, v5
	s_nop 1
	v_permlane32_swap_b32_e32 v2, v4
	v_permlane32_swap_b32_e32 v3, v5
	global_store_dwordx4 v[130:131], v[132:135], off
	global_store_dwordx4 v[130:131], v[2:5], off offset:32
.LBB0_1023:
	s_or_b64 exec, exec, s[36:37]
	v_cmp_gt_i32_e32 vcc, s50, v168
	s_and_saveexec_b64 s[36:37], vcc
	s_cbranch_execz .LBB0_1006
	v_mov_b32_e32 v2, s48

	v_add_u32_e32 v3, s49, v168
	v_mul_f32_e32 v10, 0xbfb8aa3b, v84
	v_mul_f32_e32 v11, 0xbfb8aa3b, v85
	v_mul_f32_e32 v12, 0xbfb8aa3b, v86
	s_waitcnt lgkmcnt(0)
	v_cmp_gt_i32_e32 vcc, v2, v3
	v_mul_f32_e32 v13, 0xbfb8aa3b, v87
	v_mul_f32_e32 v8, 0xbfb8aa3b, v82
	v_cndmask_b32_e64 v2, 8, 0, vcc
	v_lshl_add_u32 v4, v2, 2, s48

	v_or_b32_e32 v5, 4, v2
	v_mul_f32_e32 v9, 0xbfb8aa3b, v83
	v_exp_f32_e32 v10, v10
	v_exp_f32_e32 v11, v11
	s_waitcnt lgkmcnt(0)
	v_cmp_gt_i32_e32 vcc, v4, v3
	v_exp_f32_e32 v12, v12
	v_exp_f32_e32 v13, v13
	v_cndmask_b32_e32 v2, v5, v2, vcc
	v_lshl_add_u32 v4, v2, 2, s48

	v_or_b32_e32 v5, 2, v2
	v_exp_f32_e32 v8, v8
	v_exp_f32_e32 v9, v9
	v_mul_f32_e32 v14, 0xbfb8aa3b, v88
	s_waitcnt lgkmcnt(0)
	v_cmp_gt_i32_e32 vcc, v4, v3
	v_mul_f32_e32 v15, 0xbfb8aa3b, v89
	v_exp_f32_e32 v14, v14
	v_cndmask_b32_e32 v2, v5, v2, vcc
	v_lshl_add_u32 v4, v2, 2, s48

	v_or_b32_e32 v5, 1, v2
	v_exp_f32_e32 v15, v15
	v_add_f32_e32 v10, 1.0, v10
	v_add_f32_e32 v11, 1.0, v11
	s_waitcnt lgkmcnt(0)
	v_cmp_gt_i32_e32 vcc, v4, v3
	v_add_u32_e32 v3, s47, v3
	v_add_f32_e32 v12, 1.0, v12
	v_cndmask_b32_e32 v2, v5, v2, vcc
	v_lshl_add_u32 v4, v2, 2, s48

	v_add_f32_e32 v13, 1.0, v13
	v_add_f32_e32 v8, 1.0, v8
	v_add_f32_e32 v9, 1.0, v9
	v_rcp_f32_e32 v10, v10
	s_waitcnt lgkmcnt(0)
	v_sub_u32_e32 v3, v3, v4
	v_lshl_add_u32 v2, v2, 9, v3
	v_ashrrev_i32_e32 v3, 31, v2
	v_lshl_add_u64 v[2:3], v[2:3], 2, s[8:9]
	v_mov_b32_e32 v5, v211
	v_rcp_f32_e32 v11, v11
	v_rcp_f32_e32 v12, v12
	v_rcp_f32_e32 v13, v13
	v_rcp_f32_e32 v8, v8
	v_rcp_f32_e32 v9, v9
	v_mul_f32_e32 v16, 0xbfb8aa3b, v90
	v_mul_f32_e32 v17, 0xbfb8aa3b, v91
	v_mul_f32_e32 v18, 0xbfb8aa3b, v92
	v_exp_f32_e32 v16, v16
	v_exp_f32_e32 v17, v17
	v_exp_f32_e32 v18, v18
	v_add_f32_e32 v14, 1.0, v14
	v_add_f32_e32 v15, 1.0, v15
	v_mov_b32_e32 v4, v100
	v_rcp_f32_e32 v14, v14
	v_rcp_f32_e32 v15, v15
	v_mul_f32_e32 v154, v84, v10
	v_mul_f32_e32 v10, v85, v11
	v_mul_f32_e32 v11, v86, v12
	v_mul_f32_e32 v12, v87, v13
	v_mul_f32_e32 v8, v82, v8
	v_mul_f32_e32 v9, v83, v9
	v_mul_f32_e32 v11, v102, v11
	v_mul_f32_e32 v12, v103, v12
	v_mul_f32_e32 v8, v98, v8
	v_mul_f32_e32 v9, v99, v9
	v_mov_b32_e32 v7, v147
	v_mul_f32_e32 v19, 0xbfb8aa3b, v93
	v_add_f32_e32 v16, 1.0, v16
	v_add_f32_e32 v17, 1.0, v17
	v_add_f32_e32 v18, 1.0, v18
	v_mov_b32_e32 v6, v147
	v_exp_f32_e32 v19, v19
	v_rcp_f32_e32 v16, v16
	v_rcp_f32_e32 v17, v17
	v_rcp_f32_e32 v18, v18
	v_mul_f32_e32 v13, v88, v14
	v_mul_f32_e32 v14, v89, v15
	v_mul_f32_e32 v13, v104, v13
	v_mul_f32_e32 v14, v105, v14
	v_mul_f32_e32 v10, v101, v10
	v_add_f32_e32 v19, 1.0, v19
	v_mul_f32_e32 v15, v90, v16
	v_mul_f32_e32 v16, v91, v17
	v_mul_f32_e32 v15, v106, v15
	v_mul_f32_e32 v16, v107, v16
	v_add_u32_e32 v2, s51, v168
	v_ashrrev_i32_e32 v3, 31, v2
	v_lshlrev_b64 v[2:3], 9, v[2:3]
	v_lshl_add_u64 v[2:3], s[20:21], 0, v[2:3]
	v_lshl_add_u64 v[2:3], v[2:3], 0, s[34:35]
	v_lshl_add_u64 v[2:3], v[2:3], 0, v[150:151]
	s_waitcnt vmcnt(0)
	v_pk_mul_f32 v[4:5], v[4:5], v[154:155]
	s_nop 0
	v_mul_f32_e32 v11, v11, v5
	v_mul_f32_e32 v12, v12, v5
	v_mul_f32_e32 v8, v8, v5
	v_mul_f32_e32 v9, v9, v5
	v_med3_f32 v11, v11, s45, v170
	v_med3_f32 v12, v12, s45, v170
	v_med3_f32 v8, v8, s45, v170
	v_med3_f32 v9, v9, s45, v170
	v_cvt_pk_fp8_f32 v7, v11, v12
	v_cvt_pk_fp8_f32 v6, v8, v9
	v_mul_f32_e32 v13, v13, v5
	v_mul_f32_e32 v14, v14, v5
	v_mul_f32_e32 v4, v4, v5
	v_mul_f32_e32 v10, v10, v5
	v_med3_f32 v8, v13, s45, v170
	v_med3_f32 v9, v14, s45, v170
	v_mul_f32_e32 v12, 0xbfb8aa3b, v94
	v_med3_f32 v4, v4, s45, v170
	v_med3_f32 v10, v10, s45, v170
	v_cvt_pk_fp8_f32 v7, v8, v9 op_sel:[0,0,1]
	v_mul_f32_e32 v8, v92, v18
	v_exp_f32_e32 v12, v12
	v_cvt_pk_fp8_f32 v6, v4, v10 op_sel:[0,0,1]
	v_rcp_f32_e32 v4, v19
	v_mul_f32_e32 v8, v108, v8
	v_mul_f32_e32 v15, v15, v5
	v_mul_f32_e32 v16, v16, v5
	v_mul_f32_e32 v8, v8, v5
	v_med3_f32 v9, v15, s45, v170
	v_med3_f32 v10, v16, s45, v170
	v_med3_f32 v11, v8, s45, v170
	v_mov_b32_e32 v8, v147
	v_cvt_pk_fp8_f32 v8, v9, v10
	v_mul_f32_e32 v9, 0xbfb8aa3b, v95
	v_add_f32_e32 v10, 1.0, v12
	v_mul_f32_e32 v4, v93, v4
	v_exp_f32_e32 v9, v9
	v_rcp_f32_e32 v10, v10
	v_mul_f32_e32 v4, v109, v4
	v_mul_f32_e32 v4, v4, v5
	v_med3_f32 v4, v4, s45, v170
	v_cvt_pk_fp8_f32 v8, v11, v4 op_sel:[0,0,1]
	v_add_f32_e32 v4, 1.0, v9
	v_mul_f32_e32 v9, v94, v10
	v_mul_f32_e32 v10, 0xbfb8aa3b, v96
	v_mul_f32_e32 v11, 0xbfb8aa3b, v97
	v_exp_f32_e32 v10, v10
	v_exp_f32_e32 v11, v11
	v_rcp_f32_e32 v4, v4
	v_mul_f32_e32 v9, v110, v9
	v_add_f32_e32 v10, 1.0, v10
	v_add_f32_e32 v11, 1.0, v11
	v_mul_f32_e32 v4, v95, v4
	v_rcp_f32_e32 v10, v10
	v_rcp_f32_e32 v11, v11
	v_mul_f32_e32 v4, v111, v4
	v_mul_f32_e32 v9, v9, v5
	v_mul_f32_e32 v4, v4, v5
	v_med3_f32 v12, v9, s45, v170
	v_med3_f32 v4, v4, s45, v170
	v_mov_b32_e32 v9, v147
	v_mul_f32_e32 v10, v96, v10
	v_mul_f32_e32 v11, v97, v11
	v_cvt_pk_fp8_f32 v9, v12, v4
	v_mul_f32_e32 v10, v112, v10
	v_mul_f32_e32 v11, v113, v11
	v_mul_f32_e32 v10, v10, v5
	v_mul_f32_e32 v4, v11, v5
	v_med3_f32 v10, v10, s45, v170
	v_med3_f32 v4, v4, s45, v170
	v_cvt_pk_fp8_f32 v9, v10, v4 op_sel:[0,0,1]
	v_mul_f32_e32 v4, 0xbfb8aa3b, v50
	v_mul_f32_e32 v10, 0xbfb8aa3b, v51
	v_exp_f32_e32 v4, v4
	v_exp_f32_e32 v10, v10
	v_permlane32_swap_b32_e32 v6, v7
	v_permlane32_swap_b32_e32 v8, v9
	s_nop 1
	v_permlane32_swap_b32_e32 v6, v8
	v_permlane32_swap_b32_e32 v7, v9
	v_add_f32_e32 v4, 1.0, v4
	global_store_dwordx4 v[2:3], v[6:9], off
	v_rcp_f32_e32 v4, v4
	v_mul_f32_e32 v11, 0xbfb8aa3b, v58
	v_add_f32_e32 v6, 1.0, v10
	v_mul_f32_e32 v7, 0xbfb8aa3b, v52
	v_mul_f32_e32 v8, 0xbfb8aa3b, v53
	v_rcp_f32_e32 v6, v6
	v_exp_f32_e32 v7, v7
	v_exp_f32_e32 v8, v8
	v_mul_f32_e32 v10, 0xbfb8aa3b, v54
	v_mul_f32_e32 v4, v50, v4
	v_mul_f32_e32 v6, v51, v6
	v_add_f32_e32 v7, 1.0, v7
	v_add_f32_e32 v8, 1.0, v8
	v_exp_f32_e32 v10, v10
	v_mul_f32_e32 v4, v34, v4
	v_mul_f32_e32 v6, v35, v6
	v_rcp_f32_e32 v7, v7
	v_rcp_f32_e32 v8, v8
	v_mul_f32_e32 v4, v4, v5
	v_mul_f32_e32 v6, v6, v5
	v_med3_f32 v4, v4, s45, v170
	v_med3_f32 v9, v6, s45, v170
	v_mov_b32_e32 v6, v147
	v_cvt_pk_fp8_f32 v6, v4, v9
	v_mul_f32_e32 v4, 0xbfb8aa3b, v55
	v_add_f32_e32 v9, 1.0, v10
	v_mul_f32_e32 v7, v52, v7
	v_mul_f32_e32 v8, v53, v8
	v_exp_f32_e32 v4, v4
	v_rcp_f32_e32 v9, v9
	v_mul_f32_e32 v7, v36, v7
	v_mul_f32_e32 v8, v37, v8
	v_mul_f32_e32 v7, v7, v5
	v_mul_f32_e32 v8, v8, v5
	v_med3_f32 v7, v7, s45, v170
	v_med3_f32 v8, v8, s45, v170
	v_cvt_pk_fp8_f32 v6, v7, v8 op_sel:[0,0,1]
	v_add_f32_e32 v4, 1.0, v4
	v_mul_f32_e32 v7, v54, v9
	v_mul_f32_e32 v8, 0xbfb8aa3b, v56
	v_mul_f32_e32 v9, 0xbfb8aa3b, v57
	v_rcp_f32_e32 v4, v4
	v_exp_f32_e32 v8, v8
	v_exp_f32_e32 v9, v9
	v_exp_f32_e32 v11, v11
	v_mul_f32_e32 v4, v55, v4
	v_add_f32_e32 v8, 1.0, v8
	v_add_f32_e32 v9, 1.0, v9
	v_mul_f32_e32 v7, v38, v7
	v_mul_f32_e32 v4, v39, v4
	v_rcp_f32_e32 v8, v8
	v_rcp_f32_e32 v9, v9
	v_mul_f32_e32 v7, v7, v5
	v_mul_f32_e32 v4, v4, v5
	v_med3_f32 v10, v7, s45, v170
	v_med3_f32 v4, v4, s45, v170
	v_mov_b32_e32 v7, v147
	v_cvt_pk_fp8_f32 v7, v10, v4
	v_mul_f32_e32 v4, 0xbfb8aa3b, v59
	v_add_f32_e32 v10, 1.0, v11
	v_mul_f32_e32 v8, v56, v8
	v_mul_f32_e32 v9, v57, v9
	v_exp_f32_e32 v4, v4
	v_rcp_f32_e32 v10, v10
	v_mul_f32_e32 v8, v40, v8
	v_mul_f32_e32 v9, v41, v9
	v_mul_f32_e32 v8, v8, v5
	v_mul_f32_e32 v9, v9, v5
	v_med3_f32 v8, v8, s45, v170
	v_med3_f32 v9, v9, s45, v170
	v_cvt_pk_fp8_f32 v7, v8, v9 op_sel:[0,0,1]
	v_add_f32_e32 v4, 1.0, v4
	v_mul_f32_e32 v8, v58, v10
	v_mul_f32_e32 v9, 0xbfb8aa3b, v60
	v_mul_f32_e32 v10, 0xbfb8aa3b, v61
	v_rcp_f32_e32 v4, v4
	v_exp_f32_e32 v9, v9
	v_exp_f32_e32 v10, v10
	v_mul_f32_e32 v12, 0xbfb8aa3b, v62
	v_mul_f32_e32 v4, v59, v4
	v_add_f32_e32 v9, 1.0, v9
	v_add_f32_e32 v10, 1.0, v10
	v_exp_f32_e32 v12, v12
	v_mul_f32_e32 v8, v42, v8
	v_mul_f32_e32 v4, v43, v4
	v_rcp_f32_e32 v9, v9
	v_rcp_f32_e32 v10, v10
	v_mul_f32_e32 v8, v8, v5
	v_mul_f32_e32 v4, v4, v5
	v_med3_f32 v11, v8, s45, v170
	v_med3_f32 v4, v4, s45, v170
	v_mov_b32_e32 v8, v147
	v_cvt_pk_fp8_f32 v8, v11, v4
	v_add_f32_e32 v11, 1.0, v12
	v_mul_f32_e32 v9, v60, v9
	v_mul_f32_e32 v10, v61, v10
	v_mul_f32_e32 v4, 0xbfb8aa3b, v63
	v_rcp_f32_e32 v11, v11
	v_mul_f32_e32 v9, v44, v9
	v_mul_f32_e32 v10, v45, v10
	v_exp_f32_e32 v4, v4
	v_mul_f32_e32 v9, v9, v5
	v_mul_f32_e32 v10, v10, v5
	v_med3_f32 v9, v9, s45, v170
	v_med3_f32 v10, v10, s45, v170
	v_cvt_pk_fp8_f32 v8, v9, v10 op_sel:[0,0,1]
	v_mul_f32_e32 v9, v62, v11
	v_mul_f32_e32 v10, 0xbfb8aa3b, v64
	v_mul_f32_e32 v11, 0xbfb8aa3b, v65
	v_add_f32_e32 v4, 1.0, v4
	v_exp_f32_e32 v10, v10
	v_exp_f32_e32 v11, v11
	v_rcp_f32_e32 v4, v4
	v_mul_f32_e32 v9, v46, v9
	v_add_f32_e32 v10, 1.0, v10
	v_add_f32_e32 v11, 1.0, v11
	v_mul_f32_e32 v4, v63, v4
	v_rcp_f32_e32 v10, v10
	v_rcp_f32_e32 v11, v11
	v_mul_f32_e32 v4, v47, v4
	v_mul_f32_e32 v9, v9, v5
	v_mul_f32_e32 v4, v4, v5
	v_med3_f32 v12, v9, s45, v170
	v_med3_f32 v4, v4, s45, v170
	v_mov_b32_e32 v9, v147
	v_mul_f32_e32 v10, v64, v10
	v_mul_f32_e32 v11, v65, v11
	v_cvt_pk_fp8_f32 v9, v12, v4
	v_mul_f32_e32 v10, v48, v10
	v_mul_f32_e32 v11, v49, v11
	v_mul_f32_e32 v10, v10, v5
	v_mul_f32_e32 v4, v11, v5
	v_med3_f32 v5, v10, s45, v170
	v_med3_f32 v4, v4, s45, v170
	v_cvt_pk_fp8_f32 v9, v5, v4 op_sel:[0,0,1]
	v_permlane32_swap_b32_e32 v6, v7
	s_nop 0
	v_permlane32_swap_b32_e32 v8, v9
	s_nop 1
	v_permlane32_swap_b32_e32 v6, v8
	v_permlane32_swap_b32_e32 v7, v9
	global_store_dwordx4 v[2:3], v[6:9], off offset:32
	s_branch .LBB0_1006
